# cache-policy lever: nt hint on the once-read f32 in-projection rows read by the odd-layer c-norm pass (on top of the nt expert-weight loads)
# speedup vs baseline: 1.0026x; 1.0017x over previous
; __device__ __forceinline__ void odd_c_phase(Frame& F, KArgs a, int j) {
;     ...
;     for (int r0 = F.gw; r0 < NR; r0 += RB * F.NGW) {
;         f32x4 cq[RB]; f32x2 ckv[RB]; float kr[RB]; bool ok[RB]; int rw[RB];
; #pragma unroll
;         for (int k = 0; k < RB; ++k) { int r = r0 + k * F.NGW; ok[k] = r < NR; if (!ok[k]) r = r0; rw[k] = r;
;             const float* cr = CR + (size_t)r * 512;
;             cq[k] = *(const f32x4*)(cr + 4 * lane); ckv[k] = *(const f32x2*)(cr + 256 + 2 * lane); kr[k] = (lane < 32) ? cr[384 + lane] : 0.f; }
.LBB0_389:
	s_ashr_i32 s23, s22, 31
	s_lshl_b64 s[10:11], s[22:23], 11
	s_add_u32 s10, s25, s10
	s_addc_u32 s11, s30, s11
	v_lshlrev_b32_e32 v6, 2, v26
	global_load_dwordx4 v[18:21], v6, s[10:11] nt
	global_load_dwordx2 v[36:37], v47, s[10:11] offset:1024 nt
	v_mov_b32_e32 v50, 0
	v_lshlrev_b32_e32 v38, 2, v22
	v_mov_b32_e32 v51, 0
	s_and_saveexec_b64 s[14:15], s[4:5]
	s_cbranch_execz .LBB0_391
	global_load_dword v51, v38, s[10:11] offset:1536 nt
.LBB0_391:
	s_or_b64 exec, exec, s[14:15]
	s_add_i32 s14, s24, s22
	s_cmp_lt_i32 s14, 0x10800
	s_cselect_b64 s[52:53], -1, 0
	s_and_b64 s[10:11], s[52:53], exec
	s_cselect_b32 s50, s14, s22
	s_ashr_i32 s51, s50, 31
	s_lshl_b64 s[10:11], s[50:51], 11
	s_add_u32 s10, s25, s10
	s_addc_u32 s11, s30, s11
	s_waitcnt lgkmcnt(0)
	global_load_dwordx4 v[14:17], v6, s[10:11] nt
	global_load_dwordx2 v[34:35], v47, s[10:11] offset:1024 nt
	s_and_saveexec_b64 s[14:15], s[4:5]
	s_cbranch_execz .LBB0_393
	global_load_dword v50, v38, s[10:11] offset:1536 nt
.LBB0_393:
	s_or_b64 exec, exec, s[14:15]
	s_add_i32 s14, s38, s22
	s_cmp_lt_i32 s14, 0x10800
	s_cselect_b64 s[46:47], -1, 0
	s_and_b64 s[10:11], s[46:47], exec
	s_cselect_b32 s44, s14, s22
	s_ashr_i32 s45, s44, 31
	s_lshl_b64 s[10:11], s[44:45], 11
	s_add_u32 s10, s25, s10
	s_addc_u32 s11, s30, s11
	global_load_dwordx4 v[10:13], v6, s[10:11] nt
	global_load_dwordx2 v[32:33], v47, s[10:11] offset:1024 nt
	v_mov_b32_e32 v48, 0
	v_mov_b32_e32 v49, 0
	s_and_saveexec_b64 s[14:15], s[4:5]
	s_cbranch_execz .LBB0_395
	global_load_dword v49, v38, s[10:11] offset:1536 nt
.LBB0_395:
	s_or_b64 exec, exec, s[14:15]
	s_mul_i32 s10, s3, 24
	s_add_i32 s14, s10, s22
	s_cmp_lt_i32 s14, 0x10800
	s_cselect_b64 s[40:41], -1, 0
	s_and_b64 s[10:11], s[40:41], exec
	s_cselect_b32 s36, s14, s22
	s_ashr_i32 s37, s36, 31
	s_lshl_b64 s[10:11], s[36:37], 11
	s_add_u32 s10, s25, s10
	s_addc_u32 s11, s30, s11
	global_load_dwordx4 v[6:9], v6, s[10:11] nt
	s_nop 0
	global_load_dwordx2 v[30:31], v47, s[10:11] offset:1024 nt
	s_and_saveexec_b64 s[14:15], s[4:5]
	s_cbranch_execz .LBB0_397
	global_load_dword v48, v38, s[10:11] offset:1536 nt
